# hand-written RG-LRU phase + workgroup->(b,h,cg) map putting the four cg siblings on one XCD
# speedup vs baseline: 1.0370x; 1.0161x over previous
.LBB0_1451:
	s_load_dwordx4 s[0:3], s[8:9], 0x138
	s_waitcnt lgkmcnt(0)
	s_mov_b64 s[4:5], s[0:1]
	s_cmp_lt_i32 s4, 12
	s_cselect_b64 s[0:1], -1, 0
	s_cmp_gt_i32 s5, 11
	s_cselect_b64 s[2:3], -1, 0
	s_and_b64 s[0:1], s[0:1], s[2:3]
	s_andn2_b64 vcc, exec, s[0:1]
	s_cbranch_vccnz .LBB0_1535
	s_mov_b64 s[24:25], s[8:9]
	v_mbcnt_lo_u32_b32 v202, -1, 0
	v_mbcnt_hi_u32_b32 v202, -1, v202
	s_load_dword s0, s[8:9], 0x148
	s_waitcnt lgkmcnt(0)
	v_writelane_b32 v241, s0, 18
	s_nop 1
	v_writelane_b32 v241, s1, 19
	s_add_u32 s0, s8, 0x148
	s_addc_u32 s1, s9, 0
	v_writelane_b32 v241, s0, 34
	s_nop 1
	v_writelane_b32 v241, s1, 35
	v_readlane_b32 s0, v243, 0
	s_cmpk_gt_i32 s0, 0xff
	v_readlane_b32 s1, v243, 1
	s_cbranch_scc1 .LBB0_1482
	v_readlane_b32 s0, v243, 7
	v_readlane_b32 s1, v243, 8
	v_readlane_b32 s4, v243, 0
	v_readlane_b32 s6, v243, 12
	s_load_dwordx2 s[2:3], s[0:1], 0x130
	s_lshr_b32 s7, s6, 2
	s_and_b32 s8, s6, 3
	s_bfe_u32 s11, s4, 0x20003
	s_lshr_b32 s50, s4, 5
	s_lshl_b32 s50, s50, 3
	s_and_b32 s51, s4, 7
	s_or_b32 s50, s50, s51
	s_lshr_b32 s9, s50, 2
	s_and_b32 s10, s50, 3
	v_and_b32_e32 v160, 15, v202
	v_lshrrev_b32_e32 v161, 4, v202
	v_lshlrev_b32_e32 v209, 2, v202
	s_lshl_b32 s50, s7, 15
	v_xor_b32_e32 v178, v161, v160
	v_lshlrev_b32_e32 v178, 4, v178
	v_lshl_add_u32 v162, v160, 9, v178
	v_add_u32_e32 v162, s50, v162
	s_lshl_b32 s51, s11, 6
	s_lshl_b32 s52, s8, 4
	s_add_i32 s51, s51, s52
	v_add_u32_e32 v179, s51, v160
	v_lshrrev_b32_e32 v180, 3, v179
	v_and_b32_e32 v181, 7, v179
	v_lshlrev_b32_e32 v181, 1, v181
	v_lshlrev_b32_e32 v182, 2, v161
	v_add_u32_e32 v183, 0, v182
	v_xor_b32_e32 v184, v180, v183
	v_lshlrev_b32_e32 v184, 4, v184
	v_lshl_add_u32 v184, v183, 9, v184
	v_add3_u32 v165, v184, v181, s50
	v_add_u32_e32 v183, 1, v182
	v_xor_b32_e32 v184, v180, v183
	v_lshlrev_b32_e32 v184, 4, v184
	v_lshl_add_u32 v184, v183, 9, v184
	v_add3_u32 v166, v184, v181, s50
	v_add_u32_e32 v183, 2, v182
	v_xor_b32_e32 v184, v180, v183
	v_lshlrev_b32_e32 v184, 4, v184
	v_lshl_add_u32 v184, v183, 9, v184
	v_add3_u32 v167, v184, v181, s50
	v_add_u32_e32 v183, 3, v182
	v_xor_b32_e32 v184, v180, v183
	v_lshlrev_b32_e32 v184, 4, v184
	v_lshl_add_u32 v184, v183, 9, v184
	v_add3_u32 v168, v184, v181, s50
	v_lshrrev_b32_e32 v185, 5, v202
	v_and_b32_e32 v186, 31, v202
	s_lshl_b32 s51, s6, 4
	v_add_u32_e32 v187, 0, v185
	v_xor_b32_e32 v188, v186, v187
	v_lshlrev_b32_e32 v188, 4, v188
	v_add_u32_e32 v187, s51, v187
	v_lshl_add_u32 v211, v187, 11, v188
	v_add_u32_e32 v187, 2, v185
	v_xor_b32_e32 v188, v186, v187
	v_lshlrev_b32_e32 v188, 4, v188
	v_add_u32_e32 v187, s51, v187
	v_lshl_add_u32 v212, v187, 11, v188
	v_add_u32_e32 v187, 4, v185
	v_xor_b32_e32 v188, v186, v187
	v_lshlrev_b32_e32 v188, 4, v188
	v_add_u32_e32 v187, s51, v187
	v_lshl_add_u32 v213, v187, 11, v188
	v_add_u32_e32 v187, 6, v185
	v_xor_b32_e32 v188, v186, v187
	v_lshlrev_b32_e32 v188, 4, v188
	v_add_u32_e32 v187, s51, v187
	v_lshl_add_u32 v214, v187, 11, v188
	v_add_u32_e32 v187, 8, v185
	v_xor_b32_e32 v188, v186, v187
	v_lshlrev_b32_e32 v188, 4, v188
	v_add_u32_e32 v187, s51, v187
	v_lshl_add_u32 v215, v187, 11, v188
	v_add_u32_e32 v187, 10, v185
	v_xor_b32_e32 v188, v186, v187
	v_lshlrev_b32_e32 v188, 4, v188
	v_add_u32_e32 v187, s51, v187
	v_lshl_add_u32 v216, v187, 11, v188
	v_add_u32_e32 v187, 12, v185
	v_xor_b32_e32 v188, v186, v187
	v_lshlrev_b32_e32 v188, 4, v188
	v_add_u32_e32 v187, s51, v187
	v_lshl_add_u32 v217, v187, 11, v188
	v_add_u32_e32 v187, 14, v185
	v_xor_b32_e32 v188, v186, v187
	v_lshlrev_b32_e32 v188, 4, v188
	v_add_u32_e32 v187, s51, v187
	v_lshl_add_u32 v218, v187, 11, v188
	s_lshl_b32 s51, s6, 7
	s_add_i32 s51, s51, 0x20000
	v_lshl_add_u32 v207, v160, 3, s51
	s_lshl_b32 s51, s8, 7
	s_add_i32 s51, s51, 0x20000
	v_lshl_add_u32 v208, v160, 3, s51
	s_lshl_b32 s51, s7, 6
	v_add_u32_e32 v189, s51, v182
	s_lshl_b32 s51, s8, 4
	v_add_u32_e32 v190, s51, v160
	v_lshlrev_b32_e32 v190, 1, v190
	v_lshl_add_u32 v210, v189, 11, v190
	s_waitcnt lgkmcnt(0)
	s_lshl_b32 s50, s10, 9
	s_add_u32 s16, s2, s50
	s_addc_u32 s17, s3, 0
	s_add_u32 s16, s16, 0x1b900000
	s_addc_u32 s17, s17, 0
	s_lshl_b32 s50, s10, 9
	s_lshl_b32 s51, s11, 7
	s_add_i32 s50, s50, s51
	s_add_u32 s18, s2, s50
	s_addc_u32 s19, s3, 0
	s_add_u32 s18, s18, 0x13100000
	s_addc_u32 s19, s19, 0
	s_add_u32 s20, s2, s50
	s_addc_u32 s21, s3, 0
	s_add_u32 s20, s20, 0x29100000
	s_addc_u32 s21, s21, 0
	s_lshl_b32 s50, s4, 18
	s_add_u32 s22, s2, s50
	s_addc_u32 s23, s3, 0
	s_add_u32 s22, s22, 0x20100000
	s_addc_u32 s23, s23, 0
	s_lshl_b32 s50, s10, 10
	s_lshl_b32 s51, s11, 6
	s_add_i32 s50, s50, s51
	s_lshl_b32 s51, s8, 4
	s_add_i32 s50, s50, s51
	s_add_i32 s50, s50, 0
	s_lshl_b32 s50, s50, 9
	s_add_u32 s46, s2, s50
	s_addc_u32 s47, s3, 0
	s_add_u32 s46, s46, 0x1000000
	s_addc_u32 s47, s47, 0
	s_add_u32 s48, s46, 0x20000
	s_addc_u32 s49, s47, 0
	v_lshlrev_b32_e32 v178, 9, v160
	v_lshl_add_u32 v178, v161, 4, v178
	global_load_dwordx4 v[0:3], v178, s[46:47]
	global_load_dwordx4 v[4:7], v178, s[46:47] offset:64
	global_load_dwordx4 v[8:11], v178, s[46:47] offset:128
	global_load_dwordx4 v[12:15], v178, s[46:47] offset:192
	global_load_dwordx4 v[16:19], v178, s[46:47] offset:256
	global_load_dwordx4 v[20:23], v178, s[46:47] offset:320
	global_load_dwordx4 v[24:27], v178, s[46:47] offset:384
	global_load_dwordx4 v[28:31], v178, s[46:47] offset:448
	global_load_dwordx4 v[32:35], v178, s[48:49]
	global_load_dwordx4 v[36:39], v178, s[48:49] offset:64
	global_load_dwordx4 v[40:43], v178, s[48:49] offset:128
	global_load_dwordx4 v[44:47], v178, s[48:49] offset:192
	global_load_dwordx4 v[48:51], v178, s[48:49] offset:256
	global_load_dwordx4 v[52:55], v178, s[48:49] offset:320
	global_load_dwordx4 v[56:59], v178, s[48:49] offset:384
	global_load_dwordx4 v[60:63], v178, s[48:49] offset:448
	s_load_dwordx2 s[46:47], s[0:1], 0xa0
	s_load_dwordx2 s[48:49], s[0:1], 0xb0
	s_load_dwordx2 s[40:41], s[0:1], 0xb8
	s_lshl_b32 s50, s10, 8
	s_lshl_b32 s51, s11, 6
	s_add_i32 s50, s50, s51
	s_lshl_b32 s51, s8, 4
	s_add_i32 s50, s50, s51
	v_add_u32_e32 v179, s50, v160
	v_lshlrev_b32_e32 v179, 2, v179
	s_waitcnt lgkmcnt(0)
	global_load_dword v173, v179, s[46:47]
	global_load_dword v174, v179, s[48:49]
	global_load_dword v175, v179, s[40:41]
	v_cmp_le_u32_e64 s[34:35], 16, v202
	v_cmp_le_u32_e64 s[36:37], 32, v202
	v_add_u32_e32 v204, -16, v202
	v_add_u32_e32 v205, -32, v202
	v_add_u32_e32 v206, 48, v160
	s_cmp_eq_u32 s7, 1
	s_cselect_b64 s[38:39], -1, 0
	v_and_b32_e32 v204, 63, v204
	v_lshlrev_b32_e32 v204, 2, v204
	v_and_b32_e32 v205, 63, v205
	v_lshlrev_b32_e32 v205, 2, v205
	v_and_b32_e32 v206, 63, v206
	v_lshlrev_b32_e32 v206, 2, v206
	v_mov_b32_e32 v176, 0
	s_mov_b32 s53, 0xbfb8aa3b
	s_waitcnt vmcnt(0)
	v_mul_f32_e32 v173, s53, v173
	v_mul_f32_e32 v174, s53, v174
	v_mul_f32_e32 v175, s53, v175
	v_exp_f32_e32 v175, v175
	s_nop 0
	v_add_f32_e32 v180, 1.0, v175
	v_log_f32_e32 v180, v180
	v_mov_b32_e32 v181, 0x3eaaaaab
	v_fma_f32 v181, v175, v181, -0.5
	v_fma_f32 v181, v175, v181, 1.0
	v_mul_f32_e32 v181, v175, v181
	v_mul_f32_e32 v181, 0x3fb8aa3b, v181
	v_cmp_gt_f32_e32 vcc, 0x3cf5c28f, v175
	s_nop 1
	v_cndmask_b32_e32 v175, v180, v181, vcc
	v_mul_f32_e32 v175, 0xc1000000, v175
	s_mov_b32 s13, 0
	s_barrier
	s_cmp_lt_u32 s13, 2
	s_lshl_b32 s50, s13, 7
	s_lshl_b32 s51, s9, 8
	s_add_i32 s51, s51, 0x8000
	s_add_i32 s51, s51, s50
	s_lshl_b32 s59, s9, 11
	s_add_i32 s59, s59, s50
	s_addk_i32 s59, 0xff00
	s_cmp_lt_u32 s13, 2
	s_cselect_b32 s59, s51, s59
	s_lshl_b32 s52, s59, 11
	s_add_u32 s46, s16, s52
	s_addc_u32 s47, s17, 0
	s_lshl_b32 s52, s6, 13
	s_mov_b32 m0, s52
	s_add_i32 s52, s52, 0x400
	global_load_lds_dwordx4 v211, s[46:47]
	s_mov_b32 m0, s52
	s_add_i32 s52, s52, 0x400
	global_load_lds_dwordx4 v212, s[46:47]
	s_mov_b32 m0, s52
	s_add_i32 s52, s52, 0x400
	global_load_lds_dwordx4 v213, s[46:47]
	s_mov_b32 m0, s52
	s_add_i32 s52, s52, 0x400
	global_load_lds_dwordx4 v214, s[46:47]
	s_mov_b32 m0, s52
	s_add_i32 s52, s52, 0x400
	global_load_lds_dwordx4 v215, s[46:47]
	s_mov_b32 m0, s52
	s_add_i32 s52, s52, 0x400
	global_load_lds_dwordx4 v216, s[46:47]
	s_mov_b32 m0, s52
	s_add_i32 s52, s52, 0x400
	global_load_lds_dwordx4 v217, s[46:47]
	s_mov_b32 m0, s52
	s_nop 0
	global_load_lds_dwordx4 v218, s[46:47]
	s_waitcnt vmcnt(0)
	s_barrier
	s_cmp_eq_u32 s13, 17
	s_cbranch_scc1 .Lmylru_nodma_1
	s_add_i32 s58, s13, 1
	s_cmp_lt_u32 s58, 2
	s_lshl_b32 s50, s58, 7
	s_lshl_b32 s51, s9, 8
	s_add_i32 s51, s51, 0x8000
	s_add_i32 s51, s51, s50
	s_lshl_b32 s59, s9, 11
	s_add_i32 s59, s59, s50
	s_addk_i32 s59, 0xff00
	s_cmp_lt_u32 s58, 2
	s_cselect_b32 s59, s51, s59
	s_lshl_b32 s52, s59, 11
	s_add_u32 s46, s16, s52
	s_addc_u32 s47, s17, 0
	s_lshl_b32 s52, s6, 13
	s_add_i32 s52, s52, 0x10000
	s_mov_b32 m0, s52
	s_add_i32 s52, s52, 0x400
	global_load_lds_dwordx4 v211, s[46:47]
	s_mov_b32 m0, s52
	s_add_i32 s52, s52, 0x400
	global_load_lds_dwordx4 v212, s[46:47]
	s_mov_b32 m0, s52
	s_add_i32 s52, s52, 0x400
	global_load_lds_dwordx4 v213, s[46:47]
	s_mov_b32 m0, s52
	s_add_i32 s52, s52, 0x400
	global_load_lds_dwordx4 v214, s[46:47]
	s_mov_b32 m0, s52
	s_add_i32 s52, s52, 0x400
	global_load_lds_dwordx4 v215, s[46:47]
	s_mov_b32 m0, s52
	s_add_i32 s52, s52, 0x400
	global_load_lds_dwordx4 v216, s[46:47]
	s_mov_b32 m0, s52
	s_add_i32 s52, s52, 0x400
	global_load_lds_dwordx4 v217, s[46:47]
	s_mov_b32 m0, s52
	s_nop 0
	global_load_lds_dwordx4 v218, s[46:47]
